# k+4 weight loads and next-node bookkeeping of the first own k-step issued in the reduce read-latency shadow
# baseline (speedup 1.0000x reference)
.LBB1_2:
	v_lshrrev_b32_e32 v151, 4, v137
	s_lshl_b64 s[6:7], s[2:3], 4
	v_cmp_eq_u32_e64 s[2:3], 1, v151
	s_waitcnt vmcnt(31)
	v_cvt_f16_f32_e32 v8, v8
	v_cmp_gt_u32_e32 vcc, 16, v137
	s_waitcnt vmcnt(29)
	v_cndmask_b32_e64 v116, 0, v116, s[2:3]
	s_waitcnt vmcnt(21)
	v_cndmask_b32_e64 v100, 0, v100, s[2:3]
	v_cmp_eq_u32_e64 s[0:1], 2, v151
	v_cndmask_b32_e64 v114, 0, v114, s[2:3]
	v_cndmask_b32_e64 v115, 0, v115, s[2:3]
	v_cndmask_b32_e32 v6, v116, v6, vcc
	v_cndmask_b32_e64 v116, 0, v117, s[2:3]
	v_cndmask_b32_e64 v108, 0, v108, s[2:3]
	v_cndmask_b32_e32 v26, v100, v26, vcc
	v_cvt_f16_f32_e32 v29, v29
	v_cndmask_b32_e64 v100, 0, v101, s[2:3]
	v_cndmask_b32_e32 v28, 0, v28, vcc
	v_cndmask_b32_e64 v152, 0, 1.0, s[0:1]
	v_cndmask_b32_e32 v114, v114, v120, vcc
	v_cndmask_b32_e32 v115, v115, v121, vcc
	v_cndmask_b32_e32 v7, v116, v7, vcc
	v_cndmask_b32_e64 v106, 0, v106, s[2:3]
	v_cndmask_b32_e64 v107, 0, v107, s[2:3]
	v_cndmask_b32_e32 v14, v108, v14, vcc
	v_cndmask_b32_e64 v108, 0, v109, s[2:3]
	v_cndmask_b32_e32 v27, v100, v27, vcc
	v_cvt_f16_f32_e32 v100, v28
	v_cndmask_b32_e32 v116, 0, v8, vcc
	v_cvt_pk_f16_f32 v8, v6, v7
	v_cvt_pk_f16_f32 v7, v114, v115
	v_cndmask_b32_e64 v114, v152, v140, s[2:3]
	v_cndmask_b32_e32 v106, v106, v112, vcc
	v_cndmask_b32_e32 v107, v107, v113, vcc
	v_cndmask_b32_e32 v15, v108, v15, vcc
	v_cndmask_b32_e64 v98, 0, v98, s[2:3]
	v_cndmask_b32_e64 v99, 0, v99, s[2:3]
	v_cndmask_b32_e32 v110, v114, v110, vcc
	v_cndmask_b32_e64 v114, 0, v141, s[2:3]
	v_cndmask_b32_e32 v108, 0, v16, vcc
	v_cvt_pk_f16_f32 v16, v14, v15
	v_cvt_pk_f16_f32 v15, v106, v107
	v_cndmask_b32_e64 v106, v152, v138, s[2:3]
	v_cndmask_b32_e32 v98, v98, v104, vcc
	v_cndmask_b32_e32 v99, v99, v105, vcc
	v_cndmask_b32_e32 v111, v114, v111, vcc
	v_cndmask_b32_e32 v102, v106, v102, vcc
	v_cndmask_b32_e64 v106, 0, v139, s[2:3]
	v_cndmask_b32_e32 v29, 0, v29, vcc
	v_cvt_pk_f16_f32 v28, v26, v27
	v_cvt_pk_f16_f32 v27, v98, v99
	v_lshlrev_b32_e32 v101, 10, v1
	v_bitop3_b32 v98, v151, v0, 3 bitop3:0x78
	v_lshl_add_u64 v[130:131], s[4:5], 0, v[130:131]
	v_cvt_f16_f32_e32 v4, v4
	v_cvt_pk_f16_f32 v14, v110, v111
	v_cndmask_b32_e32 v103, v106, v103, vcc
	v_pack_b32_f16 v29, v100, v29
	v_lshl_or_b32 v111, v98, 4, v101
	v_lshlrev_b32_e32 v100, 4, v1
	s_movk_i32 s4, 0xc0
	v_cndmask_b32_e64 v124, 0, v124, s[2:3]
	v_cvt_pk_f16_f32 v26, v102, v103
	v_and_b32_e32 v112, 0xc0, v100
	v_bitop3_b32 v100, v100, s4, v111 bitop3:0x26
	s_lshl_b32 s4, s20, 3
	v_lshrrev_b32_e32 v102, 5, v137
	v_lshrrev_b32_e32 v104, 1, v137
	v_cndmask_b32_e64 v122, 0, v122, s[2:3]
	v_cndmask_b32_e64 v123, 0, v123, s[2:3]
	v_cndmask_b32_e32 v2, v124, v2, vcc
	v_cvt_f16_f32_e32 v5, v5
	v_cndmask_b32_e64 v124, 0, v125, s[2:3]
	v_cvt_f16_f32_e32 v9, v9
	v_or_b32_e32 v103, s4, v102
	v_and_or_b32 v110, v104, 8, v101
	v_bitop3_b32 v101, s4, v1, v102 bitop3:0x36
	s_lshl_b32 s4, s20, 4
	v_cndmask_b32_e32 v122, v122, v128, vcc
	v_cndmask_b32_e32 v123, v123, v129, vcc
	v_cndmask_b32_e32 v3, v124, v3, vcc
	v_cndmask_b32_e32 v17, 0, v17, vcc
	v_lshlrev_b32_e32 v107, 4, v101
	v_bitop3_b32 v101, v103, v1, 2 bitop3:0x36
	s_add_i32 s4, s4, 0x10000
	v_bfe_u32 v0, v0, 4, 2
	v_cndmask_b32_e64 v144, v152, v144, s[2:3]
	v_cndmask_b32_e32 v124, 0, v4, vcc
	v_cvt_pk_f16_f32 v4, v2, v3
	v_cvt_pk_f16_f32 v3, v122, v123
	v_cndmask_b32_e64 v122, v152, v142, s[2:3]
	v_cvt_pk_f16_f32 v17, v108, v17
	s_movk_i32 s5, 0x80
	v_lshlrev_b32_e32 v108, 4, v101
	v_bitop3_b32 v101, v103, v1, 4 bitop3:0x36
	s_cmp_lt_u32 s22, 64
	v_lshlrev_b32_e32 v104, 5, v0
	v_lshlrev_b32_e32 v0, 6, v0
	v_cndmask_b32_e32 v126, v144, v126, vcc
	v_cndmask_b32_e64 v144, 0, v145, s[2:3]
	v_cndmask_b32_e32 v118, v122, v118, vcc
	v_cndmask_b32_e64 v122, 0, v143, s[2:3]
	v_bitop3_b32 v99, v112, s5, v111 bitop3:0x36
	v_lshlrev_b32_e32 v109, 4, v101
	v_bitop3_b32 v101, v103, v1, 6 bitop3:0x36
	v_lshl_or_b32 v105, s20, 8, v0
	v_mov_b32_e32 v0, 0x1ec00
	s_cselect_b64 s[4:5], -1, 0
	v_cndmask_b32_e32 v127, v144, v127, vcc
	v_cndmask_b32_e32 v5, 0, v5, vcc
	v_cndmask_b32_e32 v119, v122, v119, vcc
	v_cndmask_b32_e32 v9, 0, v9, vcc
	v_lshlrev_b32_e32 v113, 4, v101
	v_lshlrev_b32_e32 v101, 5, v1
	v_lshl_add_u32 v106, v137, 6, v0
	s_cmp_eq_u32 s20, 0
	s_cselect_b32 s31, 0, 0xffff1d00
	v_add_u32_e32 v106, s31, v106
	v_cndmask_b32_e64 v0, 0, 1, s[4:5]
	v_lshl_add_u64 v[132:133], s[8:9], 0, v[132:133]
	v_or_b32_e32 v148, 0x400, v147
	v_or_b32_e32 v149, 0x800, v147
	v_or_b32_e32 v150, 0xc00, v147
	v_cvt_pk_f16_f32 v2, v126, v127
	v_pack_b32_f16 v5, v124, v5
	v_cvt_pk_f16_f32 v6, v118, v119
	v_pack_b32_f16 v9, v116, v9
	v_bitop3_b32 v98, v112, 64, v111 bitop3:0x36
	v_lshl_or_b32 v104, s20, 7, v104
	s_mov_b32 s22, 0x98000
	s_mov_b32 s23, 0x5040100
	s_mov_b32 s24, 0x7060302
	v_add_u32_e32 v107, v107, v110
	v_add_u32_e32 v108, v108, v110
	v_add_u32_e32 v109, v109, v110
	v_add_u32_e32 v110, v113, v110
	v_add_u32_e32 v111, v112, v111
	v_lshlrev_b32_e32 v113, 4, v137
	v_or_b32_e32 v113, 0x10000, v113
	s_lshr_b32 s28, s20, 2
	s_and_b32 s29, s20, 3
	s_lshl_b32 s28, s28, 10
	s_lshl_b32 s29, s29, 2
	s_add_i32 s28, s28, s29
	v_add_u32_e32 v112, s28, v113
	v_cmp_eq_u32_e64 s[26:27], 3, v151
	v_add_u32_e32 v114, 0x12400, v101
	v_mov_b32_e32 v121, v111
	v_mov_b32_e32 v144, v98
	v_cndmask_b32_e64 v111, v111, v99, s[84:85]
	v_cndmask_b32_e64 v99, v99, v121, s[84:85]
	v_cndmask_b32_e64 v98, v98, v100, s[84:85]
	v_cndmask_b32_e64 v100, v100, v144, s[84:85]
	v_add_u32_e32 v111, s80, v111
	v_add_u32_e32 v98, s81, v98
	v_add_u32_e32 v99, s82, v99
	v_add_u32_e32 v100, s83, v100
	v_and_b32_e32 v108, 15, v137
	s_lshl_b32 s31, s20, 3
	v_add_u32_e32 v107, s31, v151
	v_xor_b32_e32 v107, v107, v108
	v_lshlrev_b32_e32 v107, 4, v107
	v_lshl_or_b32 v107, v108, 10, v107
	v_xor_b32_e32 v108, 64, v107
	v_cmp_ne_u32_e64 s[4:5], 1, v0
	s_waitcnt vmcnt(16)
	v_cndmask_b32_e64 v1, v30, v134, s[0:1]
	v_bfi_b32 v30, s10, v1, v30
	v_perm_b32 v1, v22, v134, s24
	v_cndmask_b32_e64 v22, v22, v1, s[0:1]
	v_bfi_b32 v1, s10, v135, v18
	v_perm_b32 v121, v10, v135, s24
	v_cndmask_b32_e64 v18, v18, v1, s[0:1]
	v_cndmask_b32_e64 v10, v10, v121, s[0:1]
	v_mov_b32_e32 v121, v136
	v_mov_b32_e32 v144, v136
	v_mov_b32_e32 v145, v136
	v_mov_b32_e32 v0, v136
	v_mov_b32_e32 v1, v136
	s_waitcnt lgkmcnt(0)
	s_barrier
	ds_read_u16 v102, v114
	ds_read_u16 v103, v114 offset:512
	ds_read_u16 v115, v114 offset:1024
	ds_read_u16 v116, v114 offset:1536
	v_add_u32_e32 v0, 0x12c00, v105
	ds_read_b128 v[240:243], v0
	ds_read_b128 v[244:247], v0 offset:16
	ds_read_b128 v[248:251], v0 offset:32
	ds_read_b128 v[252:255], v0 offset:48
	v_add_u32_e32 v114, 2, v114
	s_cmp_lg_u32 s22, 0x818000
	s_cselect_b32 s9, s11, 15
	s_lshl_b32 s20, s9, 7
	s_add_i32 s25, s22, s34
	s_lshl_b32 s8, s9, 8
	buffer_load_dwordx4 v[192:195], v147, s[16:19], s25 offen
	buffer_load_dwordx4 v[196:199], v148, s[16:19], s25 offen
	buffer_load_dwordx4 v[200:203], v149, s[16:19], s25 offen
	buffer_load_dwordx4 v[204:207], v150, s[16:19], s25 offen
	s_waitcnt lgkmcnt(0)
	s_branch .LBB1_4
.LBB1_4:
	s_and_saveexec_b64 s[32:33], s[2:3]
	v_perm_b32 v5, v1, v102, s23
	v_perm_b32 v9, v121, v103, s23
	s_or_b64 exec, exec, s[32:33]
	v_mov_b32_e32 v144, v1
	v_mov_b32_e32 v145, v121
	v_mfma_f32_16x16x32_f16 v[164:167], v[30:33], v[2:5], 0
	v_mfma_f32_16x16x32_f16 v[180:183], v[22:25], v[2:5], 0
	v_permlane32_swap_b32_e32 v1, v144
	v_permlane32_swap_b32_e32 v121, v145
	v_mfma_f32_16x16x32_f16 v[168:171], v[30:33], v[6:9], 0
	v_mfma_f32_16x16x32_f16 v[184:187], v[22:25], v[6:9], 0
	s_and_saveexec_b64 s[32:33], s[2:3]
	v_perm_b32 v17, v144, v115, s23
	v_perm_b32 v29, v145, v116, s23
	s_or_b64 exec, exec, s[32:33]
	v_mfma_f32_16x16x32_f16 v[172:175], v[30:33], v[14:17], 0
	v_mfma_f32_16x16x32_f16 v[188:191], v[22:25], v[14:17], 0
	v_mfma_f32_16x16x32_f16 v[176:179], v[30:33], v[26:29], 0
	v_mfma_f32_16x16x32_f16 v[116:119], v[22:25], v[26:29], 0
	v_mfma_f32_16x16x32_f16 v[208:211], v[18:21], v[2:5], 0
	v_mfma_f32_16x16x32_f16 v[224:227], v[10:13], v[2:5], 0
	v_cvt_pk_f16_f32 v122, v164, v165
	v_cvt_pk_f16_f32 v123, v166, v167
	v_pk_max_f16 v122, v122, 0
	v_pk_max_f16 v123, v123, 0
	v_cvt_pk_f16_f32 v124, v180, v181
	v_cvt_pk_f16_f32 v125, v182, v183
	v_pk_max_f16 v124, v124, 0
	v_pk_max_f16 v125, v125, 0
	ds_write_b128 v107, v[122:125]
	v_mfma_f32_16x16x32_f16 v[212:215], v[18:21], v[6:9], 0
	v_mfma_f32_16x16x32_f16 v[228:231], v[10:13], v[6:9], 0
	v_cvt_pk_f16_f32 v126, v168, v169
	v_cvt_pk_f16_f32 v127, v170, v171
	v_pk_max_f16 v126, v126, 0
	v_pk_max_f16 v127, v127, 0
	v_cvt_pk_f16_f32 v128, v184, v185
	v_cvt_pk_f16_f32 v129, v186, v187
	v_pk_max_f16 v128, v128, 0
	v_pk_max_f16 v129, v129, 0
	ds_write_b128 v107, v[126:129] offset:16384
	v_mfma_f32_16x16x32_f16 v[216:219], v[18:21], v[14:17], 0
	v_mfma_f32_16x16x32_f16 v[232:235], v[10:13], v[14:17], 0
	v_cvt_pk_f16_f32 v134, v172, v173
	v_cvt_pk_f16_f32 v135, v174, v175
	v_pk_max_f16 v134, v134, 0
	v_pk_max_f16 v135, v135, 0
	v_cvt_pk_f16_f32 v136, v188, v189
	v_cvt_pk_f16_f32 v137, v190, v191
	v_pk_max_f16 v136, v136, 0
	v_pk_max_f16 v137, v137, 0
	ds_write_b128 v107, v[134:137] offset:32768
	v_mfma_f32_16x16x32_f16 v[220:223], v[18:21], v[26:29], 0
	v_mfma_f32_16x16x32_f16 v[236:239], v[10:13], v[26:29], 0
	v_cvt_pk_f16_f32 v138, v176, v177
	v_cvt_pk_f16_f32 v139, v178, v179
	v_pk_max_f16 v138, v138, 0
	v_pk_max_f16 v139, v139, 0
	v_cvt_pk_f16_f32 v140, v116, v117
	v_cvt_pk_f16_f32 v141, v118, v119
	v_pk_max_f16 v140, v140, 0
	v_pk_max_f16 v141, v141, 0
	ds_write_b128 v107, v[138:141] offset:49152
	v_add_u32_e32 v111, s64, v111
	v_add_u32_e32 v98, s65, v98
	v_lshl_add_u64 v[0:1], s[20:21], 3, v[132:133]
	s_waitcnt vmcnt(19)
	v_mfma_f32_16x16x32_f16 v[164:167], v[58:61], v[122:125], v[240:243]
	v_cvt_pk_f16_f32 v142, v208, v209
	v_cvt_pk_f16_f32 v143, v210, v211
	v_mfma_f32_16x16x32_f16 v[168:171], v[58:61], v[126:129], v[240:243]
	v_pk_max_f16 v142, v142, 0
	v_pk_max_f16 v143, v143, 0
	v_mfma_f32_16x16x32_f16 v[172:175], v[58:61], v[134:137], v[240:243]
	v_cvt_pk_f16_f32 v144, v224, v225
	v_cvt_pk_f16_f32 v145, v226, v227
	v_mfma_f32_16x16x32_f16 v[10:13], v[58:61], v[138:141], v[240:243]
	v_pk_max_f16 v144, v144, 0
	v_pk_max_f16 v145, v145, 0
	ds_write_b128 v108, v[142:145]
	s_waitcnt vmcnt(18)
	v_mfma_f32_16x16x32_f16 v[58:61], v[54:57], v[122:125], v[244:247]
	v_cvt_pk_f16_f32 v152, v212, v213
	v_cvt_pk_f16_f32 v153, v214, v215
	v_mfma_f32_16x16x32_f16 v[176:179], v[54:57], v[126:129], v[244:247]
	v_pk_max_f16 v152, v152, 0
	v_pk_max_f16 v153, v153, 0
	v_mfma_f32_16x16x32_f16 v[180:183], v[54:57], v[134:137], v[244:247]
	v_cvt_pk_f16_f32 v154, v228, v229
	v_cvt_pk_f16_f32 v155, v230, v231
	v_mfma_f32_16x16x32_f16 v[18:21], v[54:57], v[138:141], v[244:247]
	v_pk_max_f16 v154, v154, 0
	v_pk_max_f16 v155, v155, 0
	ds_write_b128 v108, v[152:155] offset:16384
	s_waitcnt vmcnt(17)
	v_mfma_f32_16x16x32_f16 v[54:57], v[50:53], v[122:125], v[248:251]
	v_cvt_pk_f16_f32 v156, v216, v217
	v_cvt_pk_f16_f32 v157, v218, v219
	v_mfma_f32_16x16x32_f16 v[184:187], v[50:53], v[126:129], v[248:251]
	v_pk_max_f16 v156, v156, 0
	v_pk_max_f16 v157, v157, 0
	v_mfma_f32_16x16x32_f16 v[188:191], v[50:53], v[134:137], v[248:251]
	v_cvt_pk_f16_f32 v158, v232, v233
	v_cvt_pk_f16_f32 v159, v234, v235
	v_mfma_f32_16x16x32_f16 v[22:25], v[50:53], v[138:141], v[248:251]
	v_pk_max_f16 v158, v158, 0
	v_pk_max_f16 v159, v159, 0
	ds_write_b128 v108, v[156:159] offset:32768
	s_waitcnt vmcnt(16)
	v_mfma_f32_16x16x32_f16 v[50:53], v[38:41], v[122:125], v[252:255]
	v_cvt_pk_f16_f32 v160, v220, v221
	v_cvt_pk_f16_f32 v161, v222, v223
	v_mfma_f32_16x16x32_f16 v[122:125], v[38:41], v[126:129], v[252:255]
	v_pk_max_f16 v160, v160, 0
	v_pk_max_f16 v161, v161, 0
	v_mfma_f32_16x16x32_f16 v[126:129], v[38:41], v[134:137], v[252:255]
	v_cvt_pk_f16_f32 v162, v236, v237
	v_cvt_pk_f16_f32 v163, v238, v239
	v_mfma_f32_16x16x32_f16 v[38:41], v[38:41], v[138:141], v[252:255]
	v_pk_max_f16 v162, v162, 0
	v_pk_max_f16 v163, v163, 0
	ds_write_b128 v108, v[160:163] offset:49152
	s_add_i32 s9, s22, s35
	s_waitcnt vmcnt(15)
	v_mfma_f32_16x16x32_f16 v[164:167], v[94:97], v[142:145], v[164:167]
	v_mfma_f32_16x16x32_f16 v[168:171], v[94:97], v[152:155], v[168:171]
	s_waitcnt vmcnt(14)
	v_mfma_f32_16x16x32_f16 v[58:61], v[90:93], v[142:145], v[58:61]
	v_mfma_f32_16x16x32_f16 v[176:179], v[90:93], v[152:155], v[176:179]
	s_waitcnt vmcnt(13)
	v_mfma_f32_16x16x32_f16 v[54:57], v[78:81], v[142:145], v[54:57]
	v_mfma_f32_16x16x32_f16 v[184:187], v[78:81], v[152:155], v[184:187]
	s_waitcnt vmcnt(12)
	v_mfma_f32_16x16x32_f16 v[50:53], v[34:37], v[142:145], v[50:53]
	buffer_load_dwordx4 v[140:143], v147, s[16:19], s9 offen
	buffer_load_dwordx4 v[220:223], v148, s[16:19], s9 offen
	v_mfma_f32_16x16x32_f16 v[122:125], v[34:37], v[152:155], v[122:125]
	buffer_load_dwordx4 v[152:155], v149, s[16:19], s9 offen
	buffer_load_dwordx4 v[224:227], v150, s[16:19], s9 offen
	s_mov_b32 s9, s21
	s_waitcnt lgkmcnt(0)
	s_barrier
	v_add_u32_e32 v99, s66, v99
	ds_read_b128 v[136:139], v99
	ds_read_b128 v[208:211], v99 offset:16384
	ds_read_b128 v[212:215], v99 offset:32768
	ds_read_b128 v[216:219], v99 offset:49152
	v_mfma_f32_16x16x32_f16 v[172:175], v[94:97], v[156:159], v[172:175]
	v_mfma_f32_16x16x32_f16 v[94:97], v[94:97], v[160:163], v[10:13]
	s_nop 2
	v_lshl_add_u64 v[10:11], s[8:9], 4, v[130:131]
	v_mfma_f32_16x16x32_f16 v[180:183], v[90:93], v[156:159], v[180:183]
	v_mfma_f32_16x16x32_f16 v[90:93], v[90:93], v[160:163], v[18:21]
	v_mfma_f32_16x16x32_f16 v[188:191], v[78:81], v[156:159], v[188:191]
	v_mfma_f32_16x16x32_f16 v[78:81], v[78:81], v[160:163], v[22:25]
	global_load_dwordx4 v[30:33], v[10:11], off
	s_nop 1
	global_load_dwordx4 v[22:25], v[10:11], off offset:1024
	global_load_dwordx4 v[18:21], v[10:11], off offset:2048
	s_nop 0
	global_load_dwordx4 v[10:13], v[10:11], off offset:3072
	s_nop 0
	global_load_dwordx2 v[134:135], v[0:1], off
	v_mfma_f32_16x16x32_f16 v[126:129], v[34:37], v[156:159], v[126:129]
	v_mfma_f32_16x16x32_f16 v[34:37], v[34:37], v[160:163], v[38:41]
	s_nop 2
	v_add_u32_e32 v100, s67, v100
	ds_read_b128 v[38:41], v100
	ds_read_b128 v[156:159], v100 offset:16384
	ds_read_b128 v[160:163], v100 offset:32768
	ds_read_b128 v[228:231], v100 offset:49152
	s_add_i32 s8, s22, s36
	s_waitcnt vmcnt(20) lgkmcnt(7)
	v_mfma_f32_16x16x32_f16 v[164:167], v[82:85], v[136:139], v[164:167]
	s_waitcnt lgkmcnt(6)
	v_mfma_f32_16x16x32_f16 v[168:171], v[82:85], v[208:211], v[168:171]
	s_waitcnt lgkmcnt(5)
	v_mfma_f32_16x16x32_f16 v[172:175], v[82:85], v[212:215], v[172:175]
	s_waitcnt lgkmcnt(4)
	v_mfma_f32_16x16x32_f16 v[82:85], v[82:85], v[216:219], v[94:97]
	s_waitcnt vmcnt(19)
	v_mfma_f32_16x16x32_f16 v[58:61], v[70:73], v[136:139], v[58:61]
	v_mfma_f32_16x16x32_f16 v[94:97], v[70:73], v[208:211], v[176:179]
	v_mfma_f32_16x16x32_f16 v[176:179], v[70:73], v[212:215], v[180:183]
	v_mfma_f32_16x16x32_f16 v[70:73], v[70:73], v[216:219], v[90:93]
	s_waitcnt vmcnt(18)
	v_mfma_f32_16x16x32_f16 v[54:57], v[62:65], v[136:139], v[54:57]
	v_mfma_f32_16x16x32_f16 v[90:93], v[62:65], v[208:211], v[184:187]
	v_mfma_f32_16x16x32_f16 v[180:183], v[62:65], v[212:215], v[188:191]
	v_mfma_f32_16x16x32_f16 v[62:65], v[62:65], v[216:219], v[78:81]
	s_waitcnt vmcnt(17)
	v_mfma_f32_16x16x32_f16 v[50:53], v[42:45], v[136:139], v[50:53]
	v_mfma_f32_16x16x32_f16 v[78:81], v[42:45], v[208:211], v[122:125]
	v_mfma_f32_16x16x32_f16 v[122:125], v[42:45], v[212:215], v[126:129]
	s_nop 2
	buffer_load_dwordx4 v[126:129], v147, s[16:19], s8 offen
	buffer_load_dwordx4 v[136:139], v148, s[16:19], s8 offen
	buffer_load_dwordx4 v[184:187], v149, s[16:19], s8 offen
	buffer_load_dwordx4 v[188:191], v150, s[16:19], s8 offen
	v_mfma_f32_16x16x32_f16 v[34:37], v[42:45], v[216:219], v[34:37]
	v_add_u32_e32 v111, s68, v111
	ds_read_b128 v[42:45], v111
	ds_read_b128 v[208:211], v111 offset:16384
	ds_read_b128 v[212:215], v111 offset:32768
	ds_read_b128 v[216:219], v111 offset:49152
	s_add_i32 s8, s22, s37
	s_waitcnt vmcnt(20) lgkmcnt(7)
	v_mfma_f32_16x16x32_f16 v[164:167], v[86:89], v[38:41], v[164:167]
	s_waitcnt lgkmcnt(6)
	v_mfma_f32_16x16x32_f16 v[168:171], v[86:89], v[156:159], v[168:171]
	s_waitcnt lgkmcnt(5)
	v_mfma_f32_16x16x32_f16 v[172:175], v[86:89], v[160:163], v[172:175]
	s_waitcnt lgkmcnt(4)
	v_mfma_f32_16x16x32_f16 v[82:85], v[86:89], v[228:231], v[82:85]
	s_waitcnt vmcnt(19)
	v_mfma_f32_16x16x32_f16 v[58:61], v[74:77], v[38:41], v[58:61]
	v_mfma_f32_16x16x32_f16 v[86:89], v[74:77], v[156:159], v[94:97]
	v_mfma_f32_16x16x32_f16 v[94:97], v[74:77], v[160:163], v[176:179]
	v_mfma_f32_16x16x32_f16 v[70:73], v[74:77], v[228:231], v[70:73]
	s_waitcnt vmcnt(18)
	v_mfma_f32_16x16x32_f16 v[54:57], v[66:69], v[38:41], v[54:57]
	v_mfma_f32_16x16x32_f16 v[74:77], v[66:69], v[156:159], v[90:93]
	v_mfma_f32_16x16x32_f16 v[90:93], v[66:69], v[160:163], v[180:183]
	v_mfma_f32_16x16x32_f16 v[62:65], v[66:69], v[228:231], v[62:65]
	s_waitcnt vmcnt(17)
	v_mfma_f32_16x16x32_f16 v[38:41], v[46:49], v[38:41], v[50:53]
	v_mfma_f32_16x16x32_f16 v[50:53], v[46:49], v[156:159], v[78:81]
	v_mfma_f32_16x16x32_f16 v[66:69], v[46:49], v[160:163], v[122:125]
	s_nop 1
	buffer_load_dwordx4 v[78:81], v147, s[16:19], s8 offen
	buffer_load_dwordx4 v[122:125], v148, s[16:19], s8 offen
	buffer_load_dwordx4 v[156:159], v149, s[16:19], s8 offen
	buffer_load_dwordx4 v[160:163], v150, s[16:19], s8 offen
	v_mfma_f32_16x16x32_f16 v[34:37], v[46:49], v[228:231], v[34:37]
	v_add_u32_e32 v98, s69, v98
	ds_read_b128 v[46:49], v98
	ds_read_b128 v[176:179], v98 offset:16384
	ds_read_b128 v[180:183], v98 offset:32768
	ds_read_b128 v[228:231], v98 offset:49152
	s_add_i32 s8, s22, s38
	s_waitcnt vmcnt(20) lgkmcnt(7)
	v_mfma_f32_16x16x32_f16 v[164:167], v[192:195], v[42:45], v[164:167]
	s_waitcnt lgkmcnt(6)
	v_mfma_f32_16x16x32_f16 v[168:171], v[192:195], v[208:211], v[168:171]
	s_waitcnt lgkmcnt(5)
	v_mfma_f32_16x16x32_f16 v[172:175], v[192:195], v[212:215], v[172:175]
	s_waitcnt lgkmcnt(4)
	v_mfma_f32_16x16x32_f16 v[82:85], v[192:195], v[216:219], v[82:85]
	s_waitcnt vmcnt(19)
	v_mfma_f32_16x16x32_f16 v[58:61], v[196:199], v[42:45], v[58:61]
	v_mfma_f32_16x16x32_f16 v[86:89], v[196:199], v[208:211], v[86:89]
	v_mfma_f32_16x16x32_f16 v[94:97], v[196:199], v[212:215], v[94:97]
	v_mfma_f32_16x16x32_f16 v[70:73], v[196:199], v[216:219], v[70:73]
	s_waitcnt vmcnt(18)
	v_mfma_f32_16x16x32_f16 v[54:57], v[200:203], v[42:45], v[54:57]
	v_mfma_f32_16x16x32_f16 v[74:77], v[200:203], v[208:211], v[74:77]
	v_mfma_f32_16x16x32_f16 v[90:93], v[200:203], v[212:215], v[90:93]
	v_mfma_f32_16x16x32_f16 v[62:65], v[200:203], v[216:219], v[62:65]
	s_waitcnt vmcnt(17)
	v_mfma_f32_16x16x32_f16 v[38:41], v[204:207], v[42:45], v[38:41]
	v_mfma_f32_16x16x32_f16 v[42:45], v[204:207], v[208:211], v[50:53]
	v_mfma_f32_16x16x32_f16 v[50:53], v[204:207], v[212:215], v[66:69]
	s_nop 2
	buffer_load_dwordx4 v[66:69], v147, s[16:19], s8 offen
	buffer_load_dwordx4 v[192:195], v148, s[16:19], s8 offen
	buffer_load_dwordx4 v[196:199], v149, s[16:19], s8 offen
	buffer_load_dwordx4 v[200:203], v150, s[16:19], s8 offen
	v_mfma_f32_16x16x32_f16 v[34:37], v[204:207], v[216:219], v[34:37]
	v_add_u32_e32 v99, s70, v99
	ds_read_b128 v[204:207], v99
	ds_read_b128 v[208:211], v99 offset:16384
	ds_read_b128 v[212:215], v99 offset:32768
	ds_read_b128 v[216:219], v99 offset:49152
	s_add_i32 s8, s22, s39
	s_waitcnt vmcnt(20) lgkmcnt(7)
	v_mfma_f32_16x16x32_f16 v[164:167], v[140:143], v[46:49], v[164:167]
	s_waitcnt lgkmcnt(6)
	v_mfma_f32_16x16x32_f16 v[168:171], v[140:143], v[176:179], v[168:171]
	s_waitcnt lgkmcnt(5)
	v_mfma_f32_16x16x32_f16 v[172:175], v[140:143], v[180:183], v[172:175]
	s_waitcnt lgkmcnt(4)
	v_mfma_f32_16x16x32_f16 v[82:85], v[140:143], v[228:231], v[82:85]
	s_waitcnt vmcnt(19)
	v_mfma_f32_16x16x32_f16 v[58:61], v[220:223], v[46:49], v[58:61]
	v_mfma_f32_16x16x32_f16 v[86:89], v[220:223], v[176:179], v[86:89]
	s_waitcnt vmcnt(18)
	v_mfma_f32_16x16x32_f16 v[54:57], v[152:155], v[46:49], v[54:57]
	v_mfma_f32_16x16x32_f16 v[74:77], v[152:155], v[176:179], v[74:77]
	v_mfma_f32_16x16x32_f16 v[90:93], v[152:155], v[180:183], v[90:93]
	v_mfma_f32_16x16x32_f16 v[62:65], v[152:155], v[228:231], v[62:65]
	s_waitcnt vmcnt(17)
	v_mfma_f32_16x16x32_f16 v[38:41], v[224:227], v[46:49], v[38:41]
	v_mfma_f32_16x16x32_f16 v[42:45], v[224:227], v[176:179], v[42:45]
	v_mfma_f32_16x16x32_f16 v[46:49], v[224:227], v[180:183], v[50:53]
	s_nop 2
	buffer_load_dwordx4 v[50:53], v147, s[16:19], s8 offen
	buffer_load_dwordx4 v[140:143], v148, s[16:19], s8 offen
	buffer_load_dwordx4 v[152:155], v149, s[16:19], s8 offen
	buffer_load_dwordx4 v[176:179], v150, s[16:19], s8 offen
	v_mfma_f32_16x16x32_f16 v[94:97], v[220:223], v[180:183], v[94:97]
	v_mfma_f32_16x16x32_f16 v[70:73], v[220:223], v[228:231], v[70:73]
	v_mfma_f32_16x16x32_f16 v[34:37], v[224:227], v[228:231], v[34:37]
	v_add_u32_e32 v100, s71, v100
	ds_read_b128 v[180:183], v100
	ds_read_b128 v[220:223], v100 offset:16384
	ds_read_b128 v[224:227], v100 offset:32768
	ds_read_b128 v[228:231], v100 offset:49152
	s_add_i32 s8, s22, s40
	s_waitcnt vmcnt(15) lgkmcnt(7)
	v_mfma_f32_16x16x32_f16 v[164:167], v[126:129], v[204:207], v[164:167]
	s_waitcnt lgkmcnt(6)
	v_mfma_f32_16x16x32_f16 v[168:171], v[126:129], v[208:211], v[168:171]
	s_waitcnt lgkmcnt(5)
	v_mfma_f32_16x16x32_f16 v[172:175], v[126:129], v[212:215], v[172:175]
	s_waitcnt lgkmcnt(4)
	v_mfma_f32_16x16x32_f16 v[82:85], v[126:129], v[216:219], v[82:85]
	s_waitcnt vmcnt(14)
	v_mfma_f32_16x16x32_f16 v[58:61], v[136:139], v[204:207], v[58:61]
	v_mfma_f32_16x16x32_f16 v[86:89], v[136:139], v[208:211], v[86:89]
	v_mfma_f32_16x16x32_f16 v[94:97], v[136:139], v[212:215], v[94:97]
	v_mfma_f32_16x16x32_f16 v[70:73], v[136:139], v[216:219], v[70:73]
	s_waitcnt vmcnt(13)
	v_mfma_f32_16x16x32_f16 v[54:57], v[184:187], v[204:207], v[54:57]
	v_mfma_f32_16x16x32_f16 v[74:77], v[184:187], v[208:211], v[74:77]
	v_mfma_f32_16x16x32_f16 v[90:93], v[184:187], v[212:215], v[90:93]
	v_mfma_f32_16x16x32_f16 v[62:65], v[184:187], v[216:219], v[62:65]
	s_waitcnt vmcnt(12)
	v_mfma_f32_16x16x32_f16 v[38:41], v[188:191], v[204:207], v[38:41]
	buffer_load_dwordx4 v[126:129], v147, s[16:19], s8 offen
	buffer_load_dwordx4 v[136:139], v148, s[16:19], s8 offen
	buffer_load_dwordx4 v[184:187], v149, s[16:19], s8 offen
	buffer_load_dwordx4 v[204:207], v150, s[16:19], s8 offen
	v_mfma_f32_16x16x32_f16 v[42:45], v[188:191], v[208:211], v[42:45]
	v_mfma_f32_16x16x32_f16 v[46:49], v[188:191], v[212:215], v[46:49]
	v_mfma_f32_16x16x32_f16 v[34:37], v[188:191], v[216:219], v[34:37]
	v_add_u32_e32 v111, s72, v111
	ds_read_b128 v[188:191], v111
	ds_read_b128 v[208:211], v111 offset:16384
	ds_read_b128 v[212:215], v111 offset:32768
	ds_read_b128 v[216:219], v111 offset:49152
	s_add_i32 s8, s22, s41
	s_waitcnt vmcnt(15) lgkmcnt(7)
	v_mfma_f32_16x16x32_f16 v[164:167], v[78:81], v[180:183], v[164:167]
	s_waitcnt lgkmcnt(6)
	v_mfma_f32_16x16x32_f16 v[168:171], v[78:81], v[220:223], v[168:171]
	s_waitcnt lgkmcnt(5)
	v_mfma_f32_16x16x32_f16 v[172:175], v[78:81], v[224:227], v[172:175]
	s_waitcnt lgkmcnt(4)
	v_mfma_f32_16x16x32_f16 v[78:81], v[78:81], v[228:231], v[82:85]
	s_waitcnt vmcnt(14)
	v_mfma_f32_16x16x32_f16 v[58:61], v[122:125], v[180:183], v[58:61]
	v_mfma_f32_16x16x32_f16 v[82:85], v[122:125], v[220:223], v[86:89]
	v_mfma_f32_16x16x32_f16 v[86:89], v[122:125], v[224:227], v[94:97]
	v_mfma_f32_16x16x32_f16 v[70:73], v[122:125], v[228:231], v[70:73]
	s_waitcnt vmcnt(13)
	v_mfma_f32_16x16x32_f16 v[54:57], v[156:159], v[180:183], v[54:57]
	v_mfma_f32_16x16x32_f16 v[74:77], v[156:159], v[220:223], v[74:77]
	v_mfma_f32_16x16x32_f16 v[90:93], v[156:159], v[224:227], v[90:93]
	v_mfma_f32_16x16x32_f16 v[62:65], v[156:159], v[228:231], v[62:65]
	s_waitcnt vmcnt(12)
	v_mfma_f32_16x16x32_f16 v[38:41], v[160:163], v[180:183], v[38:41]
	buffer_load_dwordx4 v[94:97], v147, s[16:19], s8 offen
	buffer_load_dwordx4 v[122:125], v148, s[16:19], s8 offen
	buffer_load_dwordx4 v[156:159], v149, s[16:19], s8 offen
	buffer_load_dwordx4 v[180:183], v150, s[16:19], s8 offen
	v_mfma_f32_16x16x32_f16 v[42:45], v[160:163], v[220:223], v[42:45]
	v_mfma_f32_16x16x32_f16 v[46:49], v[160:163], v[224:227], v[46:49]
	v_mfma_f32_16x16x32_f16 v[34:37], v[160:163], v[228:231], v[34:37]
	v_add_u32_e32 v98, s73, v98
	ds_read_b128 v[160:163], v98
	ds_read_b128 v[220:223], v98 offset:16384
	ds_read_b128 v[224:227], v98 offset:32768
	ds_read_b128 v[228:231], v98 offset:49152
	s_add_i32 s8, s22, s42
	s_waitcnt vmcnt(15) lgkmcnt(7)
	v_mfma_f32_16x16x32_f16 v[164:167], v[66:69], v[188:191], v[164:167]
	s_waitcnt lgkmcnt(6)
	v_mfma_f32_16x16x32_f16 v[168:171], v[66:69], v[208:211], v[168:171]
	s_waitcnt lgkmcnt(5)
	v_mfma_f32_16x16x32_f16 v[172:175], v[66:69], v[212:215], v[172:175]
	s_waitcnt lgkmcnt(4)
	v_mfma_f32_16x16x32_f16 v[66:69], v[66:69], v[216:219], v[78:81]
	s_waitcnt vmcnt(14)
	v_mfma_f32_16x16x32_f16 v[58:61], v[192:195], v[188:191], v[58:61]
	v_mfma_f32_16x16x32_f16 v[78:81], v[192:195], v[208:211], v[82:85]
	v_mfma_f32_16x16x32_f16 v[82:85], v[192:195], v[212:215], v[86:89]
	v_mfma_f32_16x16x32_f16 v[70:73], v[192:195], v[216:219], v[70:73]
	s_waitcnt vmcnt(13)
	v_mfma_f32_16x16x32_f16 v[54:57], v[196:199], v[188:191], v[54:57]
	v_mfma_f32_16x16x32_f16 v[74:77], v[196:199], v[208:211], v[74:77]
	v_mfma_f32_16x16x32_f16 v[86:89], v[196:199], v[212:215], v[90:93]
	v_mfma_f32_16x16x32_f16 v[62:65], v[196:199], v[216:219], v[62:65]
	s_waitcnt vmcnt(12)
	v_mfma_f32_16x16x32_f16 v[38:41], v[200:203], v[188:191], v[38:41]
	buffer_load_dwordx4 v[90:93], v147, s[16:19], s8 offen
	buffer_load_dwordx4 v[188:191], v148, s[16:19], s8 offen
	buffer_load_dwordx4 v[192:195], v149, s[16:19], s8 offen
	buffer_load_dwordx4 v[196:199], v150, s[16:19], s8 offen
	v_mfma_f32_16x16x32_f16 v[42:45], v[200:203], v[208:211], v[42:45]
	v_mfma_f32_16x16x32_f16 v[46:49], v[200:203], v[212:215], v[46:49]
	v_mfma_f32_16x16x32_f16 v[34:37], v[200:203], v[216:219], v[34:37]
	v_add_u32_e32 v99, s74, v99
	ds_read_b128 v[200:203], v99
	ds_read_b128 v[208:211], v99 offset:16384
	ds_read_b128 v[212:215], v99 offset:32768
	ds_read_b128 v[216:219], v99 offset:49152
	s_add_i32 s8, s22, s43
	s_waitcnt vmcnt(15) lgkmcnt(7)
	v_mfma_f32_16x16x32_f16 v[164:167], v[50:53], v[160:163], v[164:167]
	s_waitcnt lgkmcnt(6)
	v_mfma_f32_16x16x32_f16 v[168:171], v[50:53], v[220:223], v[168:171]
	s_waitcnt lgkmcnt(5)
	v_mfma_f32_16x16x32_f16 v[172:175], v[50:53], v[224:227], v[172:175]
	s_waitcnt lgkmcnt(4)
	v_mfma_f32_16x16x32_f16 v[50:53], v[50:53], v[228:231], v[66:69]
	s_waitcnt vmcnt(14)
	v_mfma_f32_16x16x32_f16 v[58:61], v[140:143], v[160:163], v[58:61]
	v_mfma_f32_16x16x32_f16 v[66:69], v[140:143], v[220:223], v[78:81]
	v_mfma_f32_16x16x32_f16 v[78:81], v[140:143], v[224:227], v[82:85]
	v_mfma_f32_16x16x32_f16 v[70:73], v[140:143], v[228:231], v[70:73]
	s_waitcnt vmcnt(13)
	v_mfma_f32_16x16x32_f16 v[54:57], v[152:155], v[160:163], v[54:57]
	v_mfma_f32_16x16x32_f16 v[74:77], v[152:155], v[220:223], v[74:77]
	v_mfma_f32_16x16x32_f16 v[82:85], v[152:155], v[224:227], v[86:89]
	v_mfma_f32_16x16x32_f16 v[62:65], v[152:155], v[228:231], v[62:65]
	s_waitcnt vmcnt(12)
	v_mfma_f32_16x16x32_f16 v[38:41], v[176:179], v[160:163], v[38:41]
	buffer_load_dwordx4 v[86:89], v147, s[16:19], s8 offen
	buffer_load_dwordx4 v[140:143], v148, s[16:19], s8 offen
	buffer_load_dwordx4 v[152:155], v149, s[16:19], s8 offen
	buffer_load_dwordx4 v[160:163], v150, s[16:19], s8 offen
	v_mfma_f32_16x16x32_f16 v[42:45], v[176:179], v[220:223], v[42:45]
	v_mfma_f32_16x16x32_f16 v[46:49], v[176:179], v[224:227], v[46:49]
	v_mfma_f32_16x16x32_f16 v[34:37], v[176:179], v[228:231], v[34:37]
	v_add_u32_e32 v100, s75, v100
	ds_read_b128 v[176:179], v100
	ds_read_b128 v[220:223], v100 offset:16384
	ds_read_b128 v[224:227], v100 offset:32768
	ds_read_b128 v[228:231], v100 offset:49152
	s_add_i32 s8, s22, s44
	s_waitcnt vmcnt(15) lgkmcnt(7)
	v_mfma_f32_16x16x32_f16 v[164:167], v[126:129], v[200:203], v[164:167]
	s_waitcnt lgkmcnt(6)
	v_mfma_f32_16x16x32_f16 v[168:171], v[126:129], v[208:211], v[168:171]
	s_waitcnt lgkmcnt(5)
	v_mfma_f32_16x16x32_f16 v[172:175], v[126:129], v[212:215], v[172:175]
	s_waitcnt lgkmcnt(4)
	v_mfma_f32_16x16x32_f16 v[50:53], v[126:129], v[216:219], v[50:53]
	s_waitcnt vmcnt(14)
	v_mfma_f32_16x16x32_f16 v[58:61], v[136:139], v[200:203], v[58:61]
	v_mfma_f32_16x16x32_f16 v[66:69], v[136:139], v[208:211], v[66:69]
	v_mfma_f32_16x16x32_f16 v[78:81], v[136:139], v[212:215], v[78:81]
	v_mfma_f32_16x16x32_f16 v[70:73], v[136:139], v[216:219], v[70:73]
	s_waitcnt vmcnt(13)
	v_mfma_f32_16x16x32_f16 v[54:57], v[184:187], v[200:203], v[54:57]
	v_mfma_f32_16x16x32_f16 v[74:77], v[184:187], v[208:211], v[74:77]
	v_mfma_f32_16x16x32_f16 v[82:85], v[184:187], v[212:215], v[82:85]
	v_mfma_f32_16x16x32_f16 v[62:65], v[184:187], v[216:219], v[62:65]
	s_waitcnt vmcnt(12)
	v_mfma_f32_16x16x32_f16 v[38:41], v[204:207], v[200:203], v[38:41]
	buffer_load_dwordx4 v[126:129], v147, s[16:19], s8 offen
	buffer_load_dwordx4 v[136:139], v148, s[16:19], s8 offen
	buffer_load_dwordx4 v[184:187], v149, s[16:19], s8 offen
	buffer_load_dwordx4 v[200:203], v150, s[16:19], s8 offen
	v_mfma_f32_16x16x32_f16 v[42:45], v[204:207], v[208:211], v[42:45]
	v_mfma_f32_16x16x32_f16 v[46:49], v[204:207], v[212:215], v[46:49]
	v_mfma_f32_16x16x32_f16 v[34:37], v[204:207], v[216:219], v[34:37]
	v_add_u32_e32 v111, s76, v111
	ds_read_b128 v[204:207], v111
	ds_read_b128 v[208:211], v111 offset:16384
	ds_read_b128 v[212:215], v111 offset:32768
	ds_read_b128 v[216:219], v111 offset:49152
	s_add_i32 s8, s22, s45
	s_waitcnt vmcnt(15) lgkmcnt(7)
	v_mfma_f32_16x16x32_f16 v[164:167], v[94:97], v[176:179], v[164:167]
	s_waitcnt lgkmcnt(6)
	v_mfma_f32_16x16x32_f16 v[168:171], v[94:97], v[220:223], v[168:171]
	s_waitcnt vmcnt(14)
	v_mfma_f32_16x16x32_f16 v[58:61], v[122:125], v[176:179], v[58:61]
	v_mfma_f32_16x16x32_f16 v[66:69], v[122:125], v[220:223], v[66:69]
	s_waitcnt lgkmcnt(5)
	v_mfma_f32_16x16x32_f16 v[78:81], v[122:125], v[224:227], v[78:81]
	s_waitcnt lgkmcnt(4)
	v_mfma_f32_16x16x32_f16 v[70:73], v[122:125], v[228:231], v[70:73]
	s_waitcnt vmcnt(13)
	v_mfma_f32_16x16x32_f16 v[54:57], v[156:159], v[176:179], v[54:57]
	v_mfma_f32_16x16x32_f16 v[74:77], v[156:159], v[220:223], v[74:77]
	v_mfma_f32_16x16x32_f16 v[82:85], v[156:159], v[224:227], v[82:85]
	v_mfma_f32_16x16x32_f16 v[62:65], v[156:159], v[228:231], v[62:65]
	s_waitcnt vmcnt(12)
	v_mfma_f32_16x16x32_f16 v[38:41], v[180:183], v[176:179], v[38:41]
	v_mfma_f32_16x16x32_f16 v[42:45], v[180:183], v[220:223], v[42:45]
	buffer_load_dwordx4 v[122:125], v147, s[16:19], s8 offen
	buffer_load_dwordx4 v[156:159], v148, s[16:19], s8 offen
	buffer_load_dwordx4 v[176:179], v149, s[16:19], s8 offen
	buffer_load_dwordx4 v[220:223], v150, s[16:19], s8 offen
	v_mfma_f32_16x16x32_f16 v[50:53], v[94:97], v[228:231], v[50:53]
	v_mfma_f32_16x16x32_f16 v[46:49], v[180:183], v[224:227], v[46:49]
	v_mfma_f32_16x16x32_f16 v[34:37], v[180:183], v[228:231], v[34:37]
	v_mfma_f32_16x16x32_f16 v[172:175], v[94:97], v[224:227], v[172:175]
	v_add_u32_e32 v98, s77, v98
	ds_read_b128 v[94:97], v98
	ds_read_b128 v[180:183], v98 offset:16384
	ds_read_b128 v[224:227], v98 offset:32768
	ds_read_b128 v[228:231], v98 offset:49152
	s_add_i32 s8, s22, s46
	s_waitcnt vmcnt(15) lgkmcnt(7)
	v_mfma_f32_16x16x32_f16 v[164:167], v[90:93], v[204:207], v[164:167]
	s_waitcnt lgkmcnt(6)
	v_mfma_f32_16x16x32_f16 v[168:171], v[90:93], v[208:211], v[168:171]
	s_waitcnt lgkmcnt(5)
	v_mfma_f32_16x16x32_f16 v[172:175], v[90:93], v[212:215], v[172:175]
	s_waitcnt lgkmcnt(4)
	v_mfma_f32_16x16x32_f16 v[90:93], v[90:93], v[216:219], v[50:53]
	s_waitcnt vmcnt(14)
	v_mfma_f32_16x16x32_f16 v[232:235], v[188:191], v[204:207], v[58:61]
	v_mfma_f32_16x16x32_f16 v[66:69], v[188:191], v[208:211], v[66:69]
	v_mfma_f32_16x16x32_f16 v[78:81], v[188:191], v[212:215], v[78:81]
	v_mfma_f32_16x16x32_f16 v[70:73], v[188:191], v[216:219], v[70:73]
	s_waitcnt vmcnt(13)
	v_mfma_f32_16x16x32_f16 v[188:191], v[192:195], v[204:207], v[54:57]
	v_mfma_f32_16x16x32_f16 v[74:77], v[192:195], v[208:211], v[74:77]
	v_mfma_f32_16x16x32_f16 v[82:85], v[192:195], v[212:215], v[82:85]
	v_mfma_f32_16x16x32_f16 v[62:65], v[192:195], v[216:219], v[62:65]
	s_waitcnt vmcnt(12)
	v_mfma_f32_16x16x32_f16 v[192:195], v[196:199], v[204:207], v[38:41]
	buffer_load_dwordx4 v[58:61], v147, s[16:19], s8 offen
	buffer_load_dwordx4 v[54:57], v148, s[16:19], s8 offen
	buffer_load_dwordx4 v[50:53], v149, s[16:19], s8 offen
	buffer_load_dwordx4 v[38:41], v150, s[16:19], s8 offen
	v_mfma_f32_16x16x32_f16 v[42:45], v[196:199], v[208:211], v[42:45]
	v_mfma_f32_16x16x32_f16 v[46:49], v[196:199], v[212:215], v[46:49]
	v_mfma_f32_16x16x32_f16 v[196:199], v[196:199], v[216:219], v[34:37]
	v_add_u32_e32 v99, s78, v99
	ds_read_b128 v[204:207], v99
	ds_read_b128 v[208:211], v99 offset:16384
	ds_read_b128 v[212:215], v99 offset:32768
	ds_read_b128 v[216:219], v99 offset:49152
	s_add_i32 s8, s22, s47
	s_waitcnt vmcnt(15) lgkmcnt(7)
	v_mfma_f32_16x16x32_f16 v[164:167], v[86:89], v[94:97], v[164:167]
	s_waitcnt lgkmcnt(6)
	v_mfma_f32_16x16x32_f16 v[168:171], v[86:89], v[180:183], v[168:171]
	s_waitcnt lgkmcnt(5)
	v_mfma_f32_16x16x32_f16 v[172:175], v[86:89], v[224:227], v[172:175]
	s_waitcnt lgkmcnt(4)
	v_mfma_f32_16x16x32_f16 v[86:89], v[86:89], v[228:231], v[90:93]
	s_waitcnt vmcnt(14)
	v_mfma_f32_16x16x32_f16 v[232:235], v[140:143], v[94:97], v[232:235]
	v_mfma_f32_16x16x32_f16 v[66:69], v[140:143], v[180:183], v[66:69]
	v_mfma_f32_16x16x32_f16 v[236:239], v[140:143], v[224:227], v[78:81]
	v_mfma_f32_16x16x32_f16 v[70:73], v[140:143], v[228:231], v[70:73]
	s_waitcnt vmcnt(13)
	v_mfma_f32_16x16x32_f16 v[140:143], v[152:155], v[94:97], v[188:191]
	v_mfma_f32_16x16x32_f16 v[74:77], v[152:155], v[180:183], v[74:77]
	v_mfma_f32_16x16x32_f16 v[82:85], v[152:155], v[224:227], v[82:85]
	v_mfma_f32_16x16x32_f16 v[62:65], v[152:155], v[228:231], v[62:65]
	s_waitcnt vmcnt(12)
	v_mfma_f32_16x16x32_f16 v[152:155], v[160:163], v[94:97], v[192:195]
	buffer_load_dwordx4 v[94:97], v147, s[16:19], s8 offen
	buffer_load_dwordx4 v[90:93], v148, s[16:19], s8 offen
	buffer_load_dwordx4 v[78:81], v149, s[16:19], s8 offen
	buffer_load_dwordx4 v[34:37], v150, s[16:19], s8 offen
	v_mfma_f32_16x16x32_f16 v[42:45], v[160:163], v[180:183], v[42:45]
	v_mfma_f32_16x16x32_f16 v[46:49], v[160:163], v[224:227], v[46:49]
	v_mfma_f32_16x16x32_f16 v[160:163], v[160:163], v[228:231], v[196:199]
	v_add_u32_e32 v100, s79, v100
	ds_read_b128 v[180:183], v100
	ds_read_b128 v[188:191], v100 offset:16384
	ds_read_b128 v[192:195], v100 offset:32768
	ds_read_b128 v[196:199], v100 offset:49152
	s_add_i32 s8, s22, s48
	s_waitcnt vmcnt(15) lgkmcnt(7)
	v_mfma_f32_16x16x32_f16 v[164:167], v[126:129], v[204:207], v[164:167]
	s_waitcnt lgkmcnt(6)
	v_mfma_f32_16x16x32_f16 v[168:171], v[126:129], v[208:211], v[168:171]
	s_waitcnt lgkmcnt(5)
	v_mfma_f32_16x16x32_f16 v[172:175], v[126:129], v[212:215], v[172:175]
	s_waitcnt lgkmcnt(4)
	v_mfma_f32_16x16x32_f16 v[86:89], v[126:129], v[216:219], v[86:89]
	s_waitcnt vmcnt(14)
	v_mfma_f32_16x16x32_f16 v[126:129], v[136:139], v[204:207], v[232:235]
	v_mfma_f32_16x16x32_f16 v[66:69], v[136:139], v[208:211], v[66:69]
	v_mfma_f32_16x16x32_f16 v[224:227], v[136:139], v[212:215], v[236:239]
	v_mfma_f32_16x16x32_f16 v[136:139], v[136:139], v[216:219], v[70:73]
	s_waitcnt vmcnt(13)
	v_mfma_f32_16x16x32_f16 v[140:143], v[184:187], v[204:207], v[140:143]
	v_mfma_f32_16x16x32_f16 v[74:77], v[184:187], v[208:211], v[74:77]
	v_mfma_f32_16x16x32_f16 v[228:231], v[184:187], v[212:215], v[82:85]
	v_mfma_f32_16x16x32_f16 v[184:187], v[184:187], v[216:219], v[62:65]
	s_waitcnt vmcnt(12)
	v_mfma_f32_16x16x32_f16 v[152:155], v[200:203], v[204:207], v[152:155]
	v_mfma_f32_16x16x32_f16 v[204:207], v[200:203], v[208:211], v[42:45]
	buffer_load_dwordx4 v[82:85], v147, s[16:19], s8 offen
	buffer_load_dwordx4 v[70:73], v148, s[16:19], s8 offen
	buffer_load_dwordx4 v[62:65], v149, s[16:19], s8 offen
	buffer_load_dwordx4 v[42:45], v150, s[16:19], s8 offen
	v_mfma_f32_16x16x32_f16 v[46:49], v[200:203], v[212:215], v[46:49]
	v_mfma_f32_16x16x32_f16 v[160:163], v[200:203], v[216:219], v[160:163]
	v_add_u32_e32 v0, 0x1ac00, v104
	ds_read_b128 v[240:243], v0
	ds_read_b128 v[244:247], v0 offset:16
	s_waitcnt vmcnt(12) lgkmcnt(5)
	v_mfma_f32_16x16x32_f16 v[164:167], v[122:125], v[180:183], v[164:167]
	v_mfma_f32_16x16x32_f16 v[126:129], v[156:159], v[180:183], v[126:129]
	v_mfma_f32_16x16x32_f16 v[140:143], v[176:179], v[180:183], v[140:143]
	v_mfma_f32_16x16x32_f16 v[152:155], v[220:223], v[180:183], v[152:155]
	s_waitcnt lgkmcnt(4)
	v_mfma_f32_16x16x32_f16 v[168:171], v[122:125], v[188:191], v[168:171]
	v_mfma_f32_16x16x32_f16 v[208:211], v[156:159], v[188:191], v[66:69]
	v_mfma_f32_16x16x32_f16 v[212:215], v[176:179], v[188:191], v[74:77]
	v_mfma_f32_16x16x32_f16 v[204:207], v[220:223], v[188:191], v[204:207]
	s_waitcnt lgkmcnt(3)
	v_mfma_f32_16x16x32_f16 v[172:175], v[122:125], v[192:195], v[172:175]
	v_cvt_pk_f16_f32 v232, v164, v165
	v_cvt_pk_f16_f32 v233, v166, v167
	v_pk_max_f16 v232, v232, 0
	v_pk_max_f16 v233, v233, 0
	v_mfma_f32_16x16x32_f16 v[224:227], v[156:159], v[192:195], v[224:227]
	v_cvt_pk_f16_f32 v234, v126, v127
	v_cvt_pk_f16_f32 v235, v128, v129
	v_pk_max_f16 v234, v234, 0
	v_pk_max_f16 v235, v235, 0
	v_mfma_f32_16x16x32_f16 v[228:231], v[176:179], v[192:195], v[228:231]
	v_cvt_pk_f16_f32 v236, v140, v141
	v_cvt_pk_f16_f32 v237, v142, v143
	v_pk_max_f16 v236, v236, 0
	v_pk_max_f16 v237, v237, 0
	v_mfma_f32_16x16x32_f16 v[216:219], v[220:223], v[192:195], v[46:49]
	v_cvt_pk_f16_f32 v238, v152, v153
	v_cvt_pk_f16_f32 v239, v154, v155
	v_pk_max_f16 v238, v238, 0
	v_pk_max_f16 v239, v239, 0
	s_waitcnt lgkmcnt(2)
	v_mfma_f32_16x16x32_f16 v[200:203], v[122:125], v[196:199], v[86:89]
	v_cvt_pk_f16_f32 v180, v168, v169
	v_cvt_pk_f16_f32 v181, v170, v171
	v_pk_max_f16 v180, v180, 0
	v_pk_max_f16 v181, v181, 0
	s_add_i32 s8, s22, s49
	buffer_load_dwordx4 v[86:89], v147, s[16:19], s8 offen
	buffer_load_dwordx4 v[74:77], v148, s[16:19], s8 offen
	buffer_load_dwordx4 v[66:69], v149, s[16:19], s8 offen
	buffer_load_dwordx4 v[46:49], v150, s[16:19], s8 offen
	v_mfma_f32_16x16x32_f16 v[136:139], v[156:159], v[196:199], v[136:139]
	v_cvt_pk_f16_f32 v182, v208, v209
	v_cvt_pk_f16_f32 v183, v210, v211
	v_pk_max_f16 v182, v182, 0
	v_pk_max_f16 v183, v183, 0
	s_waitcnt lgkmcnt(1)
	v_mfma_f32_16x16x32_f16 v[252:255], v[240:243], v[232:235], 0
	v_cvt_pk_f16_f32 v232, v172, v173
	v_cvt_pk_f16_f32 v233, v174, v175
	v_pk_max_f16 v232, v232, 0
	v_pk_max_f16 v233, v233, 0
	v_mfma_f32_16x16x32_f16 v[184:187], v[176:179], v[196:199], v[184:187]
	v_cvt_pk_f16_f32 v188, v212, v213
	v_cvt_pk_f16_f32 v189, v214, v215
	v_pk_max_f16 v188, v188, 0
	v_pk_max_f16 v189, v189, 0
	s_waitcnt lgkmcnt(0)
	v_mfma_f32_16x16x32_f16 v[252:255], v[244:247], v[236:239], v[252:255]
	ds_read_u16 v102, v114
	ds_read_u16 v103, v114 offset:512
	ds_read_u16 v115, v114 offset:1024
	ds_read_u16 v116, v114 offset:1536
	v_cvt_pk_f16_f32 v234, v224, v225
	v_cvt_pk_f16_f32 v235, v226, v227
	v_pk_max_f16 v234, v234, 0
	v_pk_max_f16 v235, v235, 0
	v_mfma_f32_16x16x32_f16 v[160:163], v[220:223], v[196:199], v[160:163]
	v_cvt_pk_f16_f32 v190, v204, v205
	v_cvt_pk_f16_f32 v191, v206, v207
	v_pk_max_f16 v190, v190, 0
	v_pk_max_f16 v191, v191, 0
	v_mfma_f32_16x16x32_f16 v[192:195], v[240:243], v[180:183], 0
	v_cvt_pk_f16_f32 v236, v228, v229
	v_cvt_pk_f16_f32 v237, v230, v231
	v_pk_max_f16 v236, v236, 0
	v_pk_max_f16 v237, v237, 0
	v_mfma_f32_16x16x32_f16 v[192:195], v[244:247], v[188:191], v[192:195]
	v_cvt_pk_f16_f32 v238, v216, v217
	v_cvt_pk_f16_f32 v239, v218, v219
	v_pk_max_f16 v238, v238, 0
	v_pk_max_f16 v239, v239, 0
	v_cvt_pk_f16_f32 v180, v200, v201
	v_cvt_pk_f16_f32 v181, v202, v203
	v_pk_max_f16 v180, v180, 0
	v_pk_max_f16 v181, v181, 0
	v_mfma_f32_16x16x32_f16 v[196:199], v[240:243], v[232:235], 0
	v_cvt_pk_f16_f32 v182, v136, v137
	v_cvt_pk_f16_f32 v183, v138, v139
	v_pk_max_f16 v182, v182, 0
	v_pk_max_f16 v183, v183, 0
	v_mfma_f32_16x16x32_f16 v[196:199], v[244:247], v[236:239], v[196:199]
	v_cvt_pk_f16_f32 v188, v184, v185
	v_cvt_pk_f16_f32 v189, v186, v187
	v_pk_max_f16 v188, v188, 0
	v_pk_max_f16 v189, v189, 0
	v_cvt_pk_f16_f32 v190, v160, v161
	v_cvt_pk_f16_f32 v191, v162, v163
	v_pk_max_f16 v190, v190, 0
	v_pk_max_f16 v191, v191, 0
	v_mfma_f32_16x16x32_f16 v[122:125], v[240:243], v[180:183], 0
	s_nop 0
	v_mfma_f32_16x16x32_f16 v[122:125], v[244:247], v[188:191], v[122:125]
	v_add_u32_e32 v145, 0x12c00, v105
	ds_read_b128 v[240:243], v145 offset:2048
	ds_read_b128 v[244:247], v145 offset:2064
	ds_read_b128 v[248:251], v145 offset:2080
	s_load_dword s30, s[12:13], 0x0
	v_cndmask_b32_e64 v0, v252, v192, s[2:3]
	ds_read_b128 v[252:255], v145 offset:2096
	v_cndmask_b32_e64 v0, v0, v196, s[0:1]
	v_cndmask_b32_e64 v0, v0, v122, s[26:27]
	ds_write_b32 v112, v0
	s_waitcnt vmcnt(16)
	v_cndmask_b32_e64 v1, v30, v134, s[0:1]
	v_bfi_b32 v30, s10, v1, v30
	v_perm_b32 v1, v22, v134, s24
	v_cndmask_b32_e64 v22, v22, v1, s[0:1]
	v_bfi_b32 v1, s10, v135, v18
	v_perm_b32 v121, v10, v135, s24
	v_cndmask_b32_e64 v18, v18, v1, s[0:1]
	v_cndmask_b32_e64 v10, v10, v121, s[0:1]
	s_add_i32 s22, s22, 0x80000
	s_add_i32 s11, s11, 1
	s_add_u32 s12, s12, 4
	s_addc_u32 s13, s13, 0
	v_add_u32_e32 v104, 0x400, v104
	v_add_u32_e32 v105, 0x800, v105
	v_add_u32_e32 v114, 2, v114
	s_cmp_eq_u32 s22, 0x898000
	s_waitcnt lgkmcnt(0)
	s_barrier
	ds_read_b128 v[232:235], v113
	ds_read_b128 v[236:239], v113 offset:1024
	s_cmp_lg_u32 s22, 0x818000
	s_cselect_b32 s9, s11, 15
	s_lshl_b32 s20, s9, 7
	s_add_i32 s25, s22, s34
	s_lshl_b32 s8, s9, 8
	buffer_load_dwordx4 v[192:195], v147, s[16:19], s25 offen
	buffer_load_dwordx4 v[196:199], v148, s[16:19], s25 offen
	buffer_load_dwordx4 v[200:203], v149, s[16:19], s25 offen
	buffer_load_dwordx4 v[204:207], v150, s[16:19], s25 offen
	s_cmp_eq_u32 s22, 0x898000
	s_waitcnt lgkmcnt(0)
	v_add_f32_e32 v0, v232, v233
	v_add_f32_e32 v1, v234, v235
	v_add_f32_e32 v121, v236, v237
	v_add_f32_e32 v144, v238, v239
	v_add_f32_e32 v0, v0, v1
	v_add_f32_e32 v121, v121, v144
	v_add_f32_e32 v0, v0, v121
	v_add_f32_e32 v0, s30, v0
	v_cvt_f16_f32_e32 v1, v0
	v_cvt_f16_f32_e32 v121, v0
	ds_write_b32 v106, v0
	v_add_u32_e32 v106, 4, v106
	v_permlane16_swap_b32_e32 v1, v121
	s_cbranch_scc0 .LBB1_4
